# final: baseline device code (all restructuring experiments measured flat or negative)
# speedup vs baseline: 1.0048x; 1.0048x over previous
;     __device__ __forceinline__ void operator()(g8::Acc& acc, const g8::Unit& u, int wr, int wc, int fr, int fq) const {
;         const int col0 = u.pn * 256 + wc * 32 + 8 * fq;
;         const int ord = u.flags >> 8;
;         u32x2 si[2][4];
;         if (ord < 8) {
; #pragma unroll
;             for (int ai = 0; ai < 2; ++ai)
; #pragma unroll
;                 for (int m = 0; m < 4; ++m) si[ai][m] = sl[ord * 256 + ai * 128 + wr * 64 + m * 16 + fr];
;         } else {
; #pragma unroll
;         for (int ai = 0; ai < 2; ++ai)
; #pragma unroll
;             for (int m = 0; m < 4; ++m) si[ai][m] = slot[u.pm * 256 + ai * 128 + wr * 64 + m * 16 + fr];
;         }
; #pragma unroll
;         for (int ai = 0; ai < 2; ++ai)
; #pragma unroll
;             for (int m = 0; m < 4; ++m) { const int asg = (int)si[ai][m].x;
;                 if (asg >= 0) { unsigned char* rowp = Y2 + (size_t)asg * DM + col0; const float ww = __uint_as_float(si[ai][m].y) * Y2_SCALE;
; #pragma unroll
;                     for (int bj = 0; bj < 2; ++bj) { const f32x4 v0 = acc[ai][bj][m][0] * ww, v1 = acc[ai][bj][m][1] * ww;
;                         int q0 = 0, q1 = 0;
;                         q0 = __builtin_amdgcn_cvt_pk_fp8_f32(v0[0], v0[1], q0, false); q0 = __builtin_amdgcn_cvt_pk_fp8_f32(v0[2], v0[3], q0, true);
;                         q1 = __builtin_amdgcn_cvt_pk_fp8_f32(v1[0], v1[1], q1, false); q1 = __builtin_amdgcn_cvt_pk_fp8_f32(v1[2], v1[3], q1, true);
;                         *(u32x2*)(rowp + bj * 128) = (u32x2){(unsigned)q0, (unsigned)q1}; } } }
.LBB0_1373:
	s_mov_b32 s4, 0
	s_cmpk_lt_i32 s68, 0x800
	v_mbcnt_lo_u32_b32 v2, -1, s4
	v_mbcnt_hi_u32_b32 v18, -1, v2
	v_and_b32_e32 v19, 15, v18
	s_mov_b64 s[4:5], -1
	s_cbranch_scc1 .LBB0_1375
	v_or_b32_e32 v2, s51, v19
	v_lshl_add_u32 v2, s70, 8, v2
	v_ashrrev_i32_e32 v3, 31, v2
	v_lshl_add_u64 v[4:5], v[2:3], 3, s[8:9]
	v_add_u32_e32 v6, 0x90, v2
	global_load_dwordx2 v[14:15], v[4:5], off
	global_load_dwordx2 v[16:17], v[4:5], off offset:128
	global_load_dwordx2 v[10:11], v[4:5], off offset:256
	global_load_dwordx2 v[12:13], v[4:5], off offset:384
	v_add_u32_e32 v4, 0x80, v2
	v_ashrrev_i32_e32 v7, 31, v6
	v_ashrrev_i32_e32 v5, 31, v4
	v_lshl_add_u64 v[8:9], v[6:7], 3, s[8:9]
	v_add_u32_e32 v6, 0xa0, v2
	v_add_u32_e32 v2, 0xb0, v2
	v_lshl_add_u64 v[4:5], v[4:5], 3, s[8:9]
	v_ashrrev_i32_e32 v7, 31, v6
	v_ashrrev_i32_e32 v3, 31, v2
	v_lshl_add_u64 v[20:21], v[6:7], 3, s[8:9]
	v_lshl_add_u64 v[22:23], v[2:3], 3, s[8:9]
	global_load_dwordx2 v[6:7], v[4:5], off
	s_nop 0
	global_load_dwordx2 v[8:9], v[8:9], off
	s_nop 0
	global_load_dwordx2 v[2:3], v[20:21], off
	global_load_dwordx2 v[4:5], v[22:23], off
	s_mov_b64 s[4:5], 0
.LBB0_1375:
	s_andn2_b64 vcc, exec, s[4:5]
	s_cbranch_vccnz .LBB0_1377
	s_and_b32 s4, s68, 0x1fffff00
	s_lshl_b32 s4, s4, 3
	s_add_i32 s4, s59, s4
	s_waitcnt vmcnt(0)
	v_lshl_add_u32 v2, v19, 3, s4
	ds_read2_b64 v[14:17], v2 offset1:16
	ds_read2_b64 v[10:13], v2 offset0:32 offset1:48
	ds_read2_b64 v[6:9], v2 offset0:128 offset1:144
	ds_read2_b64 v[2:5], v2 offset0:160 offset1:176
.LBB0_1377:
	s_lshl_b32 s4, s69, 8
	v_lshrrev_b32_e32 v18, 1, v18
	v_and_b32_e32 v18, 0x7ffffff8, v18
	s_or_b32 s4, s4, s52
	v_add_u32_e32 v18, s4, v18
	v_ashrrev_i32_e32 v19, 31, v18
	s_waitcnt vmcnt(0) lgkmcnt(0)
	v_cmp_lt_i32_e32 vcc, -1, v14
	s_and_saveexec_b64 s[4:5], vcc
	s_cbranch_execz .LBB0_1386
	v_mov_b32_e32 v66, v14
	v_mul_f32_e32 v14, 0x41800000, v15
	v_pk_mul_f32 v[22:23], v[98:99], v[14:15] op_sel_hi:[1,0]
	v_pk_mul_f32 v[24:25], v[94:95], v[14:15] op_sel_hi:[1,0]
	v_mov_b32_e32 v26, v67
	v_mov_b32_e32 v27, v67
	v_cvt_pk_fp8_f32 v26, v22, v23
	v_cvt_pk_fp8_f32 v27, v24, v25
	v_pk_mul_f32 v[22:23], v[100:101], v[14:15] op_sel_hi:[1,0]
	v_pk_mul_f32 v[24:25], v[96:97], v[14:15] op_sel_hi:[1,0]
	v_cvt_pk_fp8_f32 v26, v22, v23 op_sel:[0,0,1]
	v_cvt_pk_fp8_f32 v27, v24, v25 op_sel:[0,0,1]
	v_pk_mul_f32 v[22:23], v[130:131], v[14:15] op_sel_hi:[1,0]
	v_pk_mul_f32 v[24:25], v[126:127], v[14:15] op_sel_hi:[1,0]
	v_mov_b32_e32 v28, v67
	v_mov_b32_e32 v29, v67
	v_cvt_pk_fp8_f32 v28, v22, v23
	v_cvt_pk_fp8_f32 v29, v24, v25
	v_pk_mul_f32 v[22:23], v[132:133], v[14:15] op_sel_hi:[1,0]
	v_pk_mul_f32 v[14:15], v[128:129], v[14:15] op_sel_hi:[1,0]
	v_lshlrev_b64 v[20:21], 11, v[66:67]
	v_cvt_pk_fp8_f32 v28, v22, v23 op_sel:[0,0,1]
	v_cvt_pk_fp8_f32 v29, v14, v15 op_sel:[0,0,1]
	v_lshl_add_u64 v[14:15], s[10:11], 0, v[20:21]
	v_lshl_add_u64 v[14:15], v[14:15], 0, v[18:19]
	global_store_dwordx2 v[14:15], v[26:27], off
	global_store_dwordx2 v[14:15], v[28:29], off offset:128
	s_or_b64 exec, exec, s[4:5]
	v_cmp_lt_i32_e32 vcc, -1, v16
	s_and_saveexec_b64 s[4:5], vcc
	s_cbranch_execnz .LBB0_1387
